# MoE GEMMs: per-tile unit selection (32-expert search + division at every tile top) replaced by a lookup in a per-workgroup unit table computed once per phase, one unit per lane
# speedup vs baseline: 1.0062x; 1.0055x over previous
; #define PG8_STAGE_A(bufoff, soff, voff) do { _Pragma("unroll") for (int _i = 0; _i < 2; ++_i) \
;         __builtin_amdgcn_raw_ptr_buffer_load_lds(rsA, (LAS void*)(lds + (bufoff) + ldsw + _i * 8192), 16, (voff)[_i], (soff), 0, 0); } while (0)
; #define PG8_STAGE_B(bufoff, soff) do { _Pragma("unroll") for (int _i = 0; _i < 2; ++_i) \
;         __builtin_amdgcn_raw_ptr_buffer_load_lds(rsB, (LAS void*)(lds + (bufoff) + ldsw + _i * 8192), 16, voffB[_i], (soff), 0, 0); } while (0)
; #define PG8_WAIT_V(n) asm volatile("s_waitcnt vmcnt(" #n ")" ::: "memory")
; #define PG8_BAR __builtin_amdgcn_s_barrier()
; template <class Epi, class Sched, bool GATHER, bool ALIGN_EPI, bool SP2, bool FP8>
; __device__ __forceinline__ void gemm_phase(LAS unsigned char* lds, const Gemm g, const Sched& S, const Epi& E) {
;     ...
;     Unit cur, nxt; int ui = 0;
;     if (!S.next(0, cur)) return;
;     typename Epi::Pre pre{};
;     f32x4 acc[2][2][4][2];
; #pragma unroll
;     for (int a = 0; a < 2; ++a)
; #pragma unroll
;         for (int b = 0; b < 2; ++b)
; #pragma unroll
;             for (int m = 0; m < 4; ++m)
; #pragma unroll
;                 for (int n = 0; n < 2; ++n) acc[a][b][m][n] = (f32x4){0.f, 0.f, 0.f, 0.f};
;     i32x8 At[4], B0[2], B1[2];
;     int cA = GATHER ? 0 : cur.pm * tstep, cB = cur.pn * tstep;
;     ...
;         PG8_STAGE_B(PG8_SB(0, 0), cB); PG8_STAGE_A(PG8_SA(0, 0), cA, vA0); PG8_STAGE_B(PG8_SB(0, 1), cB + hstep); PG8_STAGE_A(PG8_SA(0, 1), cA, vA1);
;         if (wr == 1) PG8_BAR;
;         PG8_WAIT_V(4); PG8_BAR;
;         PG8_STAGE_B(PG8_SB(1, 0), cB + kstep); PG8_STAGE_A(PG8_SA(1, 0), cA + kstep, vA0); PG8_STAGE_B(PG8_SB(1, 1), cB + hstep + kstep);
;         PG8_WAIT_V(6); PG8_BAR;
.LBB0_923:
	s_add_u32 s26, s96, 0x3d800000
	s_addc_u32 s27, s97, 0
	s_add_u32 s28, s96, 0x500000
	s_addc_u32 s29, s97, 0
	s_add_i32 s44, s36, 0x18000
	s_or_b32 s1, s80, 0x80
	s_mov_b32 s66, s62
	s_mov_b32 s67, s63
	s_mov_b32 m0, s44
	s_add_i32 s45, s36, 0x1a000
	s_waitcnt vmcnt(2)
	s_barrier
	buffer_load_dwordx4 v173, s[64:67], s1 offen lds
	s_mov_b32 m0, s45
	s_add_i32 s46, s36, 0x8000
	buffer_load_dwordx4 v174, s[64:67], s1 offen lds
	s_mov_b32 m0, s46
	s_add_i32 s47, s36, 0xa000
	buffer_load_dwordx4 v183, s[60:63], s0 offen lds
	s_mov_b32 m0, s47
	s_add_i32 s48, s36, 0x1c000
	buffer_load_dwordx4 v185, s[60:63], s0 offen lds
	s_or_b32 s0, s80, 0x40080
	s_mov_b32 m0, s48
	s_add_i32 s49, s36, 0x1e000
	buffer_load_dwordx4 v173, s[64:67], s0 offen lds
	s_mov_b32 m0, s49
	v_lshlrev_b32_e32 v3, 6, v0
	buffer_load_dwordx4 v174, s[64:67], s0 offen lds
	v_and_b32_e32 v3, 0x3c0, v3
	v_lshlrev_b32_e32 v4, 2, v0
	v_lshl_or_b32 v3, v2, 1, v3
	s_lshl_b32 s0, s8, 13
	v_and_b32_e32 v4, 32, v4
	v_bitop3_b32 v5, s0, v3, v4 bitop3:0xf6
	s_lshl_b32 s0, s7, 5
	s_and_b32 s0, s0, 0x60
	v_mov_b32_e32 v18, 0
	s_lshl_b32 s1, s0, 7
	s_waitcnt vmcnt(6)
	s_add_i32 s51, s36, 0xc000
	v_mov_b32_e32 v20, v18
	v_mov_b32_e32 v21, v18
	v_bitop3_b32 v3, s1, v3, v4 bitop3:0xf6
	s_cmpk_lt_u32 s6, 0x100
	v_mov_b32_e32 v19, v18
	v_mov_b64_e32 v[32:33], v[20:21]
	v_mov_b64_e32 v[24:25], v[20:21]
	v_mov_b64_e32 v[28:29], v[20:21]
	s_cselect_b64 s[30:31], -1, 0
	s_add_i32 s52, s36, 0xe000
	s_ashr_i32 s53, s34, 31
	v_ashrrev_i32_e32 v165, 31, v164
	v_or_b32_e32 v175, s0, v2
	s_mov_b32 s56, 0
	s_add_i32 s57, 0, 0x27d04
	s_add_i32 s58, 0, 0x27d0c
	s_add_i32 s59, 0, 0x27d14
	s_add_i32 s83, 0, 0x27d1c
	s_add_i32 s93, 0, 0x27d24
	s_add_i32 s95, 0, 0x27d2c
	s_add_i32 s82, 0, 0x27d34
	s_add_i32 s92, 0, 0x27d3c
	s_add_i32 s20, 0, 0x27d44
	s_add_i32 s21, 0, 0x27d4c
	s_add_i32 s24, 0, 0x27d54
	s_add_i32 s68, 0, 0x27d5c
	s_add_i32 s69, 0, 0x27d64
	s_add_i32 s70, 0, 0x27d6c
	s_add_i32 s71, 0, 0x27d74
	s_add_i32 s72, 0, 0x27d7c
	v_add_u32_e32 v176, 0, v3
	v_add_u32_e32 v177, 0, v5
	s_mov_b32 s73, 0xc0e00000
	v_mov_b32_e32 v178, 0x40e00000
	v_mov_b64_e32 v[30:31], v[18:19]
	v_mov_b64_e32 v[22:23], v[18:19]
	v_mov_b64_e32 v[26:27], v[18:19]
	s_barrier
;     __device__ bool next(int i, Unit& u) const {
;         const long L = (long)i * G + c; if (L >= nwg) return false;
;         int wgid = (int)L; { const int q = nwg / NXCD, r = nwg % NXCD, xcd = wgid % NXCD, off = wgid / NXCD; wgid = (xcd < r ? xcd * (q + 1) : r * (q + 1) + (xcd - r) * q) + off; }
;         int e = 0;
;         for (int j = 1; j < NEXP; ++j) if (tile0[j] * NC <= wgid) e = j;
;         const int nr = tile0[e + 1] - tile0[e], idx = wgid - tile0[e] * NC;
;         const int r = idx % nr, cn = idx / nr;
;         u.e = __builtin_amdgcn_readfirstlane(e); u.pm = __builtin_amdgcn_readfirstlane(tile0[e] + r); u.pn = __builtin_amdgcn_readfirstlane(e * NC + cn); u.r0 = __builtin_amdgcn_readfirstlane(r * BM); return true;
	v_mbcnt_lo_u32_b32 v34, -1, 0
	v_mbcnt_hi_u32_b32 v34, -1, v34
	v_readlane_b32 s0, v245, 18
	v_readfirstlane_b32 s1, v163
	v_lshlrev_b32_e32 v35, 2, v34
	v_add_u32_e32 v35, 0x27d00, v35
	ds_read_b32 v36, v35
	s_nop 1
	v_mov_b32_e32 v37, s0
	v_mad_u32_u24 v37, v34, s34, v37
	v_and_b32_e32 v38, 7, v37
	v_lshrrev_b32_e32 v39, 3, v37
	s_nop 0
	v_mad_u32_u24 v38, v38, s1, v39
	v_mov_b32_e32 v40, 0
	s_waitcnt lgkmcnt(0)
	v_lshlrev_b32_e32 v36, 4, v36
	s_nop 3
	v_readlane_b32 s32, v36, 1
	s_nop 1
	v_cmp_le_u32_e32 vcc, s32, v38
	s_nop 1
	v_cndmask_b32_e64 v40, v40, 1, vcc
	v_readlane_b32 s32, v36, 2
	s_nop 1
	v_cmp_le_u32_e32 vcc, s32, v38
	s_nop 1
	v_cndmask_b32_e64 v40, v40, 2, vcc
	v_readlane_b32 s32, v36, 3
	s_nop 1
	v_cmp_le_u32_e32 vcc, s32, v38
	s_nop 1
	v_cndmask_b32_e64 v40, v40, 3, vcc
	v_readlane_b32 s32, v36, 4
	s_nop 1
	v_cmp_le_u32_e32 vcc, s32, v38
	s_nop 1
	v_cndmask_b32_e64 v40, v40, 4, vcc
	v_readlane_b32 s32, v36, 5
	s_nop 1
	v_cmp_le_u32_e32 vcc, s32, v38
	s_nop 1
	v_cndmask_b32_e64 v40, v40, 5, vcc
	v_readlane_b32 s32, v36, 6
	s_nop 1
	v_cmp_le_u32_e32 vcc, s32, v38
	s_nop 1
	v_cndmask_b32_e64 v40, v40, 6, vcc
	v_readlane_b32 s32, v36, 7
	s_nop 1
	v_cmp_le_u32_e32 vcc, s32, v38
	s_nop 1
	v_cndmask_b32_e64 v40, v40, 7, vcc
	v_readlane_b32 s32, v36, 8
	s_nop 1
	v_cmp_le_u32_e32 vcc, s32, v38
	s_nop 1
	v_cndmask_b32_e64 v40, v40, 8, vcc
	v_readlane_b32 s32, v36, 9
	s_nop 1
	v_cmp_le_u32_e32 vcc, s32, v38
	s_nop 1
	v_cndmask_b32_e64 v40, v40, 9, vcc
	v_readlane_b32 s32, v36, 10
	s_nop 1
	v_cmp_le_u32_e32 vcc, s32, v38
	s_nop 1
	v_cndmask_b32_e64 v40, v40, 10, vcc
	v_readlane_b32 s32, v36, 11
	s_nop 1
	v_cmp_le_u32_e32 vcc, s32, v38
	s_nop 1
	v_cndmask_b32_e64 v40, v40, 11, vcc
	v_readlane_b32 s32, v36, 12
	s_nop 1
	v_cmp_le_u32_e32 vcc, s32, v38
	s_nop 1
	v_cndmask_b32_e64 v40, v40, 12, vcc
	v_readlane_b32 s32, v36, 13
	s_nop 1
	v_cmp_le_u32_e32 vcc, s32, v38
	s_nop 1
	v_cndmask_b32_e64 v40, v40, 13, vcc
	v_readlane_b32 s32, v36, 14
	s_nop 1
	v_cmp_le_u32_e32 vcc, s32, v38
	s_nop 1
	v_cndmask_b32_e64 v40, v40, 14, vcc
	v_readlane_b32 s32, v36, 15
	s_nop 1
	v_cmp_le_u32_e32 vcc, s32, v38
	s_nop 1
	v_cndmask_b32_e64 v40, v40, 15, vcc
	v_readlane_b32 s32, v36, 16
	s_nop 1
	v_cmp_le_u32_e32 vcc, s32, v38
	s_nop 1
	v_cndmask_b32_e64 v40, v40, 16, vcc
	v_readlane_b32 s32, v36, 17
	s_nop 1
	v_cmp_le_u32_e32 vcc, s32, v38
	s_nop 1
	v_cndmask_b32_e64 v40, v40, 17, vcc
	v_readlane_b32 s32, v36, 18
	s_nop 1
	v_cmp_le_u32_e32 vcc, s32, v38
	s_nop 1
	v_cndmask_b32_e64 v40, v40, 18, vcc
	v_readlane_b32 s32, v36, 19
	s_nop 1
	v_cmp_le_u32_e32 vcc, s32, v38
	s_nop 1
	v_cndmask_b32_e64 v40, v40, 19, vcc
	v_readlane_b32 s32, v36, 20
	s_nop 1
	v_cmp_le_u32_e32 vcc, s32, v38
	s_nop 1
	v_cndmask_b32_e64 v40, v40, 20, vcc
	v_readlane_b32 s32, v36, 21
	s_nop 1
	v_cmp_le_u32_e32 vcc, s32, v38
	s_nop 1
	v_cndmask_b32_e64 v40, v40, 21, vcc
	v_readlane_b32 s32, v36, 22
	s_nop 1
	v_cmp_le_u32_e32 vcc, s32, v38
	s_nop 1
	v_cndmask_b32_e64 v40, v40, 22, vcc
	v_readlane_b32 s32, v36, 23
	s_nop 1
	v_cmp_le_u32_e32 vcc, s32, v38
	s_nop 1
	v_cndmask_b32_e64 v40, v40, 23, vcc
	v_readlane_b32 s32, v36, 24
	s_nop 1
	v_cmp_le_u32_e32 vcc, s32, v38
	s_nop 1
	v_cndmask_b32_e64 v40, v40, 24, vcc
	v_readlane_b32 s32, v36, 25
	s_nop 1
	v_cmp_le_u32_e32 vcc, s32, v38
	s_nop 1
	v_cndmask_b32_e64 v40, v40, 25, vcc
	v_readlane_b32 s32, v36, 26
	s_nop 1
	v_cmp_le_u32_e32 vcc, s32, v38
	s_nop 1
	v_cndmask_b32_e64 v40, v40, 26, vcc
	v_readlane_b32 s32, v36, 27
	s_nop 1
	v_cmp_le_u32_e32 vcc, s32, v38
	s_nop 1
	v_cndmask_b32_e64 v40, v40, 27, vcc
	v_readlane_b32 s32, v36, 28
	s_nop 1
	v_cmp_le_u32_e32 vcc, s32, v38
	s_nop 1
	v_cndmask_b32_e64 v40, v40, 28, vcc
	v_readlane_b32 s32, v36, 29
	s_nop 1
	v_cmp_le_u32_e32 vcc, s32, v38
	s_nop 1
	v_cndmask_b32_e64 v40, v40, 29, vcc
	v_readlane_b32 s32, v36, 30
	s_nop 1
	v_cmp_le_u32_e32 vcc, s32, v38
	s_nop 1
	v_cndmask_b32_e64 v40, v40, 30, vcc
	v_readlane_b32 s32, v36, 31
	s_nop 1
	v_cmp_le_u32_e32 vcc, s32, v38
	s_nop 1
	v_cndmask_b32_e64 v40, v40, 31, vcc
	v_lshlrev_b32_e32 v41, 2, v40
	v_add_u32_e32 v41, 0x27d00, v41
	ds_read2_b32 v[42:43], v41 offset1:1
	s_waitcnt lgkmcnt(0)
	v_sub_u32_e32 v44, v43, v42
	v_lshlrev_b32_e32 v45, 4, v42
	v_sub_u32_e32 v45, v38, v45
	v_mov_b32_e32 v46, 0
	v_mov_b32_e32 v47, 0
	v_add_u32_e32 v47, v47, v44
	v_cmp_le_u32_e32 vcc, v47, v45
	s_nop 1
	v_addc_co_u32_e32 v46, vcc, 0, v46, vcc
	v_add_u32_e32 v47, v47, v44
	v_cmp_le_u32_e32 vcc, v47, v45
	s_nop 1
	v_addc_co_u32_e32 v46, vcc, 0, v46, vcc
	v_add_u32_e32 v47, v47, v44
	v_cmp_le_u32_e32 vcc, v47, v45
	s_nop 1
	v_addc_co_u32_e32 v46, vcc, 0, v46, vcc
	v_add_u32_e32 v47, v47, v44
	v_cmp_le_u32_e32 vcc, v47, v45
	s_nop 1
	v_addc_co_u32_e32 v46, vcc, 0, v46, vcc
	v_add_u32_e32 v47, v47, v44
	v_cmp_le_u32_e32 vcc, v47, v45
	s_nop 1
	v_addc_co_u32_e32 v46, vcc, 0, v46, vcc
	v_add_u32_e32 v47, v47, v44
	v_cmp_le_u32_e32 vcc, v47, v45
	s_nop 1
	v_addc_co_u32_e32 v46, vcc, 0, v46, vcc
	v_add_u32_e32 v47, v47, v44
	v_cmp_le_u32_e32 vcc, v47, v45
	s_nop 1
	v_addc_co_u32_e32 v46, vcc, 0, v46, vcc
	v_add_u32_e32 v47, v47, v44
	v_cmp_le_u32_e32 vcc, v47, v45
	s_nop 1
	v_addc_co_u32_e32 v46, vcc, 0, v46, vcc
	v_add_u32_e32 v47, v47, v44
	v_cmp_le_u32_e32 vcc, v47, v45
	s_nop 1
	v_addc_co_u32_e32 v46, vcc, 0, v46, vcc
	v_add_u32_e32 v47, v47, v44
	v_cmp_le_u32_e32 vcc, v47, v45
	s_nop 1
	v_addc_co_u32_e32 v46, vcc, 0, v46, vcc
	v_add_u32_e32 v47, v47, v44
	v_cmp_le_u32_e32 vcc, v47, v45
	s_nop 1
	v_addc_co_u32_e32 v46, vcc, 0, v46, vcc
	v_add_u32_e32 v47, v47, v44
	v_cmp_le_u32_e32 vcc, v47, v45
	s_nop 1
	v_addc_co_u32_e32 v46, vcc, 0, v46, vcc
	v_add_u32_e32 v47, v47, v44
	v_cmp_le_u32_e32 vcc, v47, v45
	s_nop 1
	v_addc_co_u32_e32 v46, vcc, 0, v46, vcc
	v_add_u32_e32 v47, v47, v44
	v_cmp_le_u32_e32 vcc, v47, v45
	s_nop 1
	v_addc_co_u32_e32 v46, vcc, 0, v46, vcc
	v_add_u32_e32 v47, v47, v44
	v_cmp_le_u32_e32 vcc, v47, v45
	s_nop 1
	v_addc_co_u32_e32 v46, vcc, 0, v46, vcc
	v_mul_u32_u24_e32 v48, v46, v44
	v_sub_u32_e32 v48, v45, v48
	v_mov_b32_e32 v50, v40
	v_add_u32_e32 v51, v42, v48
	v_lshl_add_u32 v52, v40, 4, v46
	v_lshlrev_b32_e32 v53, 8, v48
	v_lshlrev_b32_e32 v49, 4, v34
	v_add_u32_e32 v49, 0x20000, v49
	ds_write_b128 v49, v[50:53]
	s_waitcnt lgkmcnt(0)
	s_branch .LBB0_926

;     __device__ bool next(int i, Unit& u) const {
;         const long L = (long)i * G + c; if (L >= nwg) return false;
;         int wgid = (int)L; { const int q = nwg / NXCD, r = nwg % NXCD, xcd = wgid % NXCD, off = wgid / NXCD; wgid = (xcd < r ? xcd * (q + 1) : r * (q + 1) + (xcd - r) * q) + off; }
;         int e = 0;
;         for (int j = 1; j < NEXP; ++j) if (tile0[j] * NC <= wgid) e = j;
;         const int nr = tile0[e + 1] - tile0[e], idx = wgid - tile0[e] * NC;
;         const int r = idx % nr, cn = idx / nr;
;         u.e = __builtin_amdgcn_readfirstlane(e); u.pm = __builtin_amdgcn_readfirstlane(tile0[e] + r); u.pn = __builtin_amdgcn_readfirstlane(e * NC + cn); u.r0 = __builtin_amdgcn_readfirstlane(r * BM); return true;
.LBB0_926:
	s_add_i32 s56, s56, 1
	s_mul_i32 s0, s56, s53
	s_mul_hi_u32 s1, s56, s34
	s_add_i32 s1, s1, s0
	s_mul_i32 s0, s56, s34
	v_readlane_b32 s2, v245, 18
	s_add_u32 s0, s0, s2
	s_addc_u32 s1, s1, s35
	v_cmp_ge_i64_e32 vcc, s[0:1], v[164:165]
	v_cmp_lt_i64_e64 s[2:3], s[0:1], v[164:165]
	s_cbranch_vccnz .LBB0_928
	s_lshl_b32 s0, s56, 4
	s_add_i32 s0, s0, 0x20000
	v_mov_b32_e32 v2, s0
	ds_read_b128 v[2:5], v2
	s_waitcnt lgkmcnt(0)
	v_readfirstlane_b32 s74, v2
	v_readfirstlane_b32 s75, v3
	v_readfirstlane_b32 s76, v4
	v_readfirstlane_b32 s77, v5

; #define PG8_STAGE_A(bufoff, soff, voff) do { _Pragma("unroll") for (int _i = 0; _i < 2; ++_i) \
;         __builtin_amdgcn_raw_ptr_buffer_load_lds(rsA, (LAS void*)(lds + (bufoff) + ldsw + _i * 8192), 16, (voff)[_i], (soff), 0, 0); } while (0)
; #define PG8_STAGE_B(bufoff, soff) do { _Pragma("unroll") for (int _i = 0; _i < 2; ++_i) \
;         __builtin_amdgcn_raw_ptr_buffer_load_lds(rsB, (LAS void*)(lds + (bufoff) + ldsw + _i * 8192), 16, voffB[_i], (soff), 0, 0); } while (0)
; #define PG8_WAIT_V(n) asm volatile("s_waitcnt vmcnt(" #n ")" ::: "memory")
; #define PG8_BAR __builtin_amdgcn_s_barrier()
; template <class Epi, class Sched, bool GATHER, bool ALIGN_EPI, bool SP2, bool FP8>
; __device__ __forceinline__ void gemm_phase(LAS unsigned char* lds, const Gemm g, const Sched& S, const Epi& E) {
;     ...
;     Unit cur, nxt; int ui = 0;
;     if (!S.next(0, cur)) return;
;     typename Epi::Pre pre{};
;     f32x4 acc[2][2][4][2];
; #pragma unroll
;     for (int a = 0; a < 2; ++a)
; #pragma unroll
;         for (int b = 0; b < 2; ++b)
; #pragma unroll
;             for (int m = 0; m < 4; ++m)
; #pragma unroll
;                 for (int n = 0; n < 2; ++n) acc[a][b][m][n] = (f32x4){0.f, 0.f, 0.f, 0.f};
;     i32x8 At[4], B0[2], B1[2];
;     int cA = GATHER ? 0 : cur.pm * tstep, cB = cur.pn * tstep;
;     ...
;         PG8_STAGE_B(PG8_SB(0, 0), cB); PG8_STAGE_A(PG8_SA(0, 0), cA, vA0); PG8_STAGE_B(PG8_SB(0, 1), cB + hstep); PG8_STAGE_A(PG8_SA(0, 1), cA, vA1);
;         if (wr == 1) PG8_BAR;
;         PG8_WAIT_V(4); PG8_BAR;
;         PG8_STAGE_B(PG8_SB(1, 0), cB + kstep); PG8_STAGE_A(PG8_SA(1, 0), cA + kstep, vA0); PG8_STAGE_B(PG8_SB(1, 1), cB + hstep + kstep);
;         PG8_WAIT_V(6); PG8_BAR;
.LBB0_999:
	s_lshl_b32 s67, s10, 8
	s_add_u32 s14, s96, 0x4f800000
	s_addc_u32 s15, s97, 0
	s_add_i32 s28, s20, 0x18000
	s_or_b32 s17, s70, 0x80
	s_mov_b32 s10, s6
	s_mov_b32 s11, s7
	s_mov_b32 m0, s28
	s_add_i32 s29, s20, 0x1a000
	s_waitcnt vmcnt(2)
	s_barrier
	buffer_load_dwordx4 v163, s[8:11], s17 offen lds
	s_mov_b32 m0, s29
	s_add_i32 s30, s20, 0x8000
	buffer_load_dwordx4 v168, s[8:11], s17 offen lds
	s_or_b32 s17, s69, 0x80
	s_mov_b32 m0, s30
	s_add_i32 s31, s20, 0xa000
	buffer_load_dwordx4 v170, s[4:7], s17 offen lds
	s_mov_b32 m0, s31
	s_add_i32 s34, s20, 0x1c000
	buffer_load_dwordx4 v171, s[4:7], s17 offen lds
	s_or_b32 s17, s70, 0x40080
	s_mov_b32 m0, s34
	s_add_i32 s35, s20, 0x1e000
	buffer_load_dwordx4 v163, s[8:11], s17 offen lds
	s_mov_b32 m0, s35
	v_lshlrev_b32_e32 v3, 6, v0
	buffer_load_dwordx4 v168, s[8:11], s17 offen lds
	v_and_b32_e32 v3, 0x3c0, v3
	v_lshlrev_b32_e32 v4, 2, v0
	s_lshl_b32 s1, s1, 5
	v_lshl_or_b32 v3, v2, 1, v3
	s_lshl_b32 s10, s16, 13
	v_and_b32_e32 v4, 32, v4
	s_and_b32 s1, s1, 0x60
	v_mov_b32_e32 v18, 0
	v_bitop3_b32 v5, s10, v3, v4 bitop3:0xf6
	s_lshl_b32 s10, s1, 7
	s_waitcnt vmcnt(6)
	s_add_i32 s36, s20, 0xc000
	v_mov_b32_e32 v20, v18
	v_mov_b32_e32 v21, v18
	v_bitop3_b32 v3, s10, v3, v4 bitop3:0xf6
	s_cmpk_lt_u32 s0, 0x100
	v_mov_b32_e32 v19, v18
	v_mov_b64_e32 v[32:33], v[20:21]
	v_mov_b64_e32 v[24:25], v[20:21]
	v_mov_b64_e32 v[28:29], v[20:21]
	s_cselect_b64 s[16:17], -1, 0
	s_add_i32 s37, s20, 0xe000
	s_ashr_i32 s38, s94, 31
	v_ashrrev_i32_e32 v165, 31, v164
	v_or_b32_e32 v174, s1, v2
	s_mov_b32 s39, 0
	s_add_i32 s40, 0, 0x27d04
	s_add_i32 s41, 0, 0x27d0c
	s_add_i32 s42, 0, 0x27d14
	s_add_i32 s43, 0, 0x27d1c
	s_add_i32 s44, 0, 0x27d24
	s_add_i32 s45, 0, 0x27d2c
	s_add_i32 s46, 0, 0x27d34
	s_add_i32 s47, 0, 0x27d3c
	s_add_i32 s48, 0, 0x27d44
	s_add_i32 s49, 0, 0x27d4c
	s_add_i32 s50, 0, 0x27d54
	s_add_i32 s51, 0, 0x27d5c
	s_add_i32 s52, 0, 0x27d64
	s_add_i32 s53, 0, 0x27d6c
	s_add_i32 s56, 0, 0x27d74
	s_add_i32 s57, 0, 0x27d7c
	v_add_u32_e32 v175, 0, v3
	v_add_u32_e32 v176, 0, v5
	s_mov_b32 s18, 0x3c800000
	v_mov_b64_e32 v[30:31], v[18:19]
	v_mov_b64_e32 v[22:23], v[18:19]
	v_mov_b64_e32 v[26:27], v[18:19]
	s_barrier
;     __device__ bool next(int i, Unit& u) const {
;         const long L = (long)i * G + c; if (L >= nwg) return false;
;         int wgid = (int)L; { const int q = nwg / NXCD, r = nwg % NXCD, xcd = wgid % NXCD, off = wgid / NXCD; wgid = (xcd < r ? xcd * (q + 1) : r * (q + 1) + (xcd - r) * q) + off; }
;         int e = 0;
;         for (int j = 1; j < NEXP; ++j) if (tile0[j] * NC <= wgid) e = j;
;         const int nr = tile0[e + 1] - tile0[e], idx = wgid - tile0[e] * NC;
;         const int r = idx % nr, cn = idx / nr;
;         u.e = __builtin_amdgcn_readfirstlane(e); u.pm = __builtin_amdgcn_readfirstlane(tile0[e] + r); u.pn = __builtin_amdgcn_readfirstlane(e * NC + cn); u.r0 = __builtin_amdgcn_readfirstlane(r * BM); return true;
	v_mbcnt_lo_u32_b32 v34, -1, 0
	v_mbcnt_hi_u32_b32 v34, -1, v34
	v_readlane_b32 s10, v245, 18
	v_readfirstlane_b32 s11, v1
	v_lshlrev_b32_e32 v35, 2, v34
	v_add_u32_e32 v35, 0x27d00, v35
	ds_read_b32 v36, v35
	s_nop 1
	v_mov_b32_e32 v37, s10
	v_mad_u32_u24 v37, v34, s94, v37
	v_and_b32_e32 v38, 7, v37
	v_lshrrev_b32_e32 v39, 3, v37
	s_nop 0
	v_mad_u32_u24 v38, v38, s11, v39
	v_mov_b32_e32 v40, 0
	s_waitcnt lgkmcnt(0)
	v_lshlrev_b32_e32 v36, 3, v36
	s_nop 3
	v_readlane_b32 s32, v36, 1
	s_nop 1
	v_cmp_le_u32_e32 vcc, s32, v38
	s_nop 1
	v_cndmask_b32_e64 v40, v40, 1, vcc
	v_readlane_b32 s32, v36, 2
	s_nop 1
	v_cmp_le_u32_e32 vcc, s32, v38
	s_nop 1
	v_cndmask_b32_e64 v40, v40, 2, vcc
	v_readlane_b32 s32, v36, 3
	s_nop 1
	v_cmp_le_u32_e32 vcc, s32, v38
	s_nop 1
	v_cndmask_b32_e64 v40, v40, 3, vcc
	v_readlane_b32 s32, v36, 4
	s_nop 1
	v_cmp_le_u32_e32 vcc, s32, v38
	s_nop 1
	v_cndmask_b32_e64 v40, v40, 4, vcc
	v_readlane_b32 s32, v36, 5
	s_nop 1
	v_cmp_le_u32_e32 vcc, s32, v38
	s_nop 1
	v_cndmask_b32_e64 v40, v40, 5, vcc
	v_readlane_b32 s32, v36, 6
	s_nop 1
	v_cmp_le_u32_e32 vcc, s32, v38
	s_nop 1
	v_cndmask_b32_e64 v40, v40, 6, vcc
	v_readlane_b32 s32, v36, 7
	s_nop 1
	v_cmp_le_u32_e32 vcc, s32, v38
	s_nop 1
	v_cndmask_b32_e64 v40, v40, 7, vcc
	v_readlane_b32 s32, v36, 8
	s_nop 1
	v_cmp_le_u32_e32 vcc, s32, v38
	s_nop 1
	v_cndmask_b32_e64 v40, v40, 8, vcc
	v_readlane_b32 s32, v36, 9
	s_nop 1
	v_cmp_le_u32_e32 vcc, s32, v38
	s_nop 1
	v_cndmask_b32_e64 v40, v40, 9, vcc
	v_readlane_b32 s32, v36, 10
	s_nop 1
	v_cmp_le_u32_e32 vcc, s32, v38
	s_nop 1
	v_cndmask_b32_e64 v40, v40, 10, vcc
	v_readlane_b32 s32, v36, 11
	s_nop 1
	v_cmp_le_u32_e32 vcc, s32, v38
	s_nop 1
	v_cndmask_b32_e64 v40, v40, 11, vcc
	v_readlane_b32 s32, v36, 12
	s_nop 1
	v_cmp_le_u32_e32 vcc, s32, v38
	s_nop 1
	v_cndmask_b32_e64 v40, v40, 12, vcc
	v_readlane_b32 s32, v36, 13
	s_nop 1
	v_cmp_le_u32_e32 vcc, s32, v38
	s_nop 1
	v_cndmask_b32_e64 v40, v40, 13, vcc
	v_readlane_b32 s32, v36, 14
	s_nop 1
	v_cmp_le_u32_e32 vcc, s32, v38
	s_nop 1
	v_cndmask_b32_e64 v40, v40, 14, vcc
	v_readlane_b32 s32, v36, 15
	s_nop 1
	v_cmp_le_u32_e32 vcc, s32, v38
	s_nop 1
	v_cndmask_b32_e64 v40, v40, 15, vcc
	v_readlane_b32 s32, v36, 16
	s_nop 1
	v_cmp_le_u32_e32 vcc, s32, v38
	s_nop 1
	v_cndmask_b32_e64 v40, v40, 16, vcc
	v_readlane_b32 s32, v36, 17
	s_nop 1
	v_cmp_le_u32_e32 vcc, s32, v38
	s_nop 1
	v_cndmask_b32_e64 v40, v40, 17, vcc
	v_readlane_b32 s32, v36, 18
	s_nop 1
	v_cmp_le_u32_e32 vcc, s32, v38
	s_nop 1
	v_cndmask_b32_e64 v40, v40, 18, vcc
	v_readlane_b32 s32, v36, 19
	s_nop 1
	v_cmp_le_u32_e32 vcc, s32, v38
	s_nop 1
	v_cndmask_b32_e64 v40, v40, 19, vcc
	v_readlane_b32 s32, v36, 20
	s_nop 1
	v_cmp_le_u32_e32 vcc, s32, v38
	s_nop 1
	v_cndmask_b32_e64 v40, v40, 20, vcc
	v_readlane_b32 s32, v36, 21
	s_nop 1
	v_cmp_le_u32_e32 vcc, s32, v38
	s_nop 1
	v_cndmask_b32_e64 v40, v40, 21, vcc
	v_readlane_b32 s32, v36, 22
	s_nop 1
	v_cmp_le_u32_e32 vcc, s32, v38
	s_nop 1
	v_cndmask_b32_e64 v40, v40, 22, vcc
	v_readlane_b32 s32, v36, 23
	s_nop 1
	v_cmp_le_u32_e32 vcc, s32, v38
	s_nop 1
	v_cndmask_b32_e64 v40, v40, 23, vcc
	v_readlane_b32 s32, v36, 24
	s_nop 1
	v_cmp_le_u32_e32 vcc, s32, v38
	s_nop 1
	v_cndmask_b32_e64 v40, v40, 24, vcc
	v_readlane_b32 s32, v36, 25
	s_nop 1
	v_cmp_le_u32_e32 vcc, s32, v38
	s_nop 1
	v_cndmask_b32_e64 v40, v40, 25, vcc
	v_readlane_b32 s32, v36, 26
	s_nop 1
	v_cmp_le_u32_e32 vcc, s32, v38
	s_nop 1
	v_cndmask_b32_e64 v40, v40, 26, vcc
	v_readlane_b32 s32, v36, 27
	s_nop 1
	v_cmp_le_u32_e32 vcc, s32, v38
	s_nop 1
	v_cndmask_b32_e64 v40, v40, 27, vcc
	v_readlane_b32 s32, v36, 28
	s_nop 1
	v_cmp_le_u32_e32 vcc, s32, v38
	s_nop 1
	v_cndmask_b32_e64 v40, v40, 28, vcc
	v_readlane_b32 s32, v36, 29
	s_nop 1
	v_cmp_le_u32_e32 vcc, s32, v38
	s_nop 1
	v_cndmask_b32_e64 v40, v40, 29, vcc
	v_readlane_b32 s32, v36, 30
	s_nop 1
	v_cmp_le_u32_e32 vcc, s32, v38
	s_nop 1
	v_cndmask_b32_e64 v40, v40, 30, vcc
	v_readlane_b32 s32, v36, 31
	s_nop 1
	v_cmp_le_u32_e32 vcc, s32, v38
	s_nop 1
	v_cndmask_b32_e64 v40, v40, 31, vcc
	v_lshlrev_b32_e32 v41, 2, v40
	v_add_u32_e32 v41, 0x27d00, v41
	ds_read2_b32 v[42:43], v41 offset1:1
	s_waitcnt lgkmcnt(0)
	v_sub_u32_e32 v44, v43, v42
	v_lshlrev_b32_e32 v45, 3, v42
	v_sub_u32_e32 v45, v38, v45
	v_mov_b32_e32 v46, 0
	v_mov_b32_e32 v47, 0
	v_add_u32_e32 v47, v47, v44
	v_cmp_le_u32_e32 vcc, v47, v45
	s_nop 1
	v_addc_co_u32_e32 v46, vcc, 0, v46, vcc
	v_add_u32_e32 v47, v47, v44
	v_cmp_le_u32_e32 vcc, v47, v45
	s_nop 1
	v_addc_co_u32_e32 v46, vcc, 0, v46, vcc
	v_add_u32_e32 v47, v47, v44
	v_cmp_le_u32_e32 vcc, v47, v45
	s_nop 1
	v_addc_co_u32_e32 v46, vcc, 0, v46, vcc
	v_add_u32_e32 v47, v47, v44
	v_cmp_le_u32_e32 vcc, v47, v45
	s_nop 1
	v_addc_co_u32_e32 v46, vcc, 0, v46, vcc
	v_add_u32_e32 v47, v47, v44
	v_cmp_le_u32_e32 vcc, v47, v45
	s_nop 1
	v_addc_co_u32_e32 v46, vcc, 0, v46, vcc
	v_add_u32_e32 v47, v47, v44
	v_cmp_le_u32_e32 vcc, v47, v45
	s_nop 1
	v_addc_co_u32_e32 v46, vcc, 0, v46, vcc
	v_add_u32_e32 v47, v47, v44
	v_cmp_le_u32_e32 vcc, v47, v45
	s_nop 1
	v_addc_co_u32_e32 v46, vcc, 0, v46, vcc
	v_mul_u32_u24_e32 v48, v46, v44
	v_sub_u32_e32 v48, v45, v48
	v_mov_b32_e32 v50, v40
	v_add_u32_e32 v51, v42, v48
	v_lshl_add_u32 v52, v40, 3, v46
	v_lshlrev_b32_e32 v53, 8, v48
	v_lshlrev_b32_e32 v49, 4, v34
	v_add_u32_e32 v49, 0x20000, v49
	ds_write_b128 v49, v[50:53]
	s_waitcnt lgkmcnt(0)
	s_branch .LBB0_1002

;     __device__ bool next(int i, Unit& u) const {
;         const long L = (long)i * G + c; if (L >= nwg) return false;
;         int wgid = (int)L; { const int q = nwg / NXCD, r = nwg % NXCD, xcd = wgid % NXCD, off = wgid / NXCD; wgid = (xcd < r ? xcd * (q + 1) : r * (q + 1) + (xcd - r) * q) + off; }
;         int e = 0;
;         for (int j = 1; j < NEXP; ++j) if (tile0[j] * NC <= wgid) e = j;
;         const int nr = tile0[e + 1] - tile0[e], idx = wgid - tile0[e] * NC;
;         const int r = idx % nr, cn = idx / nr;
;         u.e = __builtin_amdgcn_readfirstlane(e); u.pm = __builtin_amdgcn_readfirstlane(tile0[e] + r); u.pn = __builtin_amdgcn_readfirstlane(e * NC + cn); u.r0 = __builtin_amdgcn_readfirstlane(r * BM); return true;
.LBB0_1002:
	s_add_i32 s39, s39, 1
	s_mul_i32 s0, s39, s38
	s_mul_hi_u32 s1, s39, s94
	s_add_i32 s1, s1, s0
	s_mul_i32 s0, s39, s94
	v_readlane_b32 s10, v245, 18
	s_add_u32 s10, s0, s10
	s_addc_u32 s11, s1, s19
	v_cmp_ge_i64_e32 vcc, s[10:11], v[164:165]
	v_cmp_lt_i64_e64 s[0:1], s[10:11], v[164:165]
	s_cbranch_vccnz .LBB0_1004
	s_lshl_b32 s10, s39, 4
	s_add_i32 s10, s10, 0x20000
	v_mov_b32_e32 v2, s10
	ds_read_b128 v[2:5], v2
	s_waitcnt lgkmcnt(0)
	v_readfirstlane_b32 s58, v2
	v_readfirstlane_b32 s59, v3
	v_readfirstlane_b32 s60, v4
	v_readfirstlane_b32 s61, v5
